# P8 epilogue: clamps fused into the bias pk_fma (clamp bit on acc*(s/R)+(b-lo)/R, then t*R+lo in one pk_fma; the +1 of the up branch folded): 96 VALU fewer per lane and unit
# speedup vs baseline: 1.0216x; 1.0216x over previous
; #define PG8_STAGE(bufoff, gbase, voff) do { PG8_GLDS((const char*)(gbase), (voff)[0], ldsb + (bufoff)); PG8_GLDS((const char*)(gbase), (voff)[1], ldsb + (bufoff) + 8192u); } while (0)
; #define PG8_STAGEA(bufoff, gbase, o0, o1) do { PG8_GLDS((const char*)(gbase), (o0), ldsb + (bufoff)); PG8_GLDS((const char*)(gbase), (o1), ldsb + (bufoff) + 8192u); } while (0)
; #define PG8_STAGEA1(bufoff, gbase) do { if constexpr (Sched::GATHER) { PG8_STAGEA(bufoff, gbase, vA2, vA3); } else { PG8_STAGEA(bufoff, (gbase) + hstep, vA0, vA1); } } while (0)
; #define PG8_WAIT_V(n) asm volatile("s_waitcnt vmcnt(" #n ")" ::: "memory")
; #define PG8_BAR __builtin_amdgcn_s_barrier()
; template <class Epi, class Sched, bool F8 = false, bool PF = false, bool I8 = false, int PID = -1>
; __device__ __forceinline__ void gemm_phase(LAS unsigned char* lds, LAS unsigned char* xlds, const int RP, const int RPB, const int nt, const Sched& S, const Epi& E, const int stagger_ticks) {
;     ...
;     PG8_ZERO_ACC();
;     PG8_STAGE(PG8_SB(0, 0), cB, voffB); PG8_STAGE(PG8_SB(0, 1), cB + hstepB, voffB); PG8_STAGEA(PG8_SA(0, 0), cA, vA0, vA1); PG8_STAGEA1(PG8_SA(0, 1), cA);
;     if (wr == 1) PG8_BAR;
;     PG8_WAIT_V(2); PG8_BAR;
;     PG8_STAGE(PG8_SB(1, 0), cB + kstep, voffB); PG8_STAGEA(PG8_SA(1, 0), cA + kstep, vA0, vA1); PG8_STAGE(PG8_SB(1, 1), cB + hstepB + kstep, voffB);
;     PG8_WAIT_V(6); PG8_BAR;
;     static __device__ __forceinline__ f32x2 act2(f32x2 g, f32x2 u) {
;         g.x = __builtin_amdgcn_fmed3f(g.x, -24.0f, 7.0f); g.y = __builtin_amdgcn_fmed3f(g.y, -24.0f, 7.0f);
;         u.x = __builtin_amdgcn_fmed3f(u.x, -7.0f, 7.0f); u.y = __builtin_amdgcn_fmed3f(u.y, -7.0f, 7.0f);
;         f32x2 z = g * (-1.702f * 1.4426950408889634f);
;         f32x2 d; d.x = __builtin_amdgcn_exp2f(z.x); d.y = __builtin_amdgcn_exp2f(z.y);
;         d = d + 1.0f;
;         const float r = __builtin_amdgcn_rcpf(d.x * d.y);
;         f32x2 sg; sg.x = r * d.y; sg.y = r * d.x;
;         return (u + 1.0f) * (g * sg);
.LBB0_954:
	v_and_b32_e32 v2, 48, v6
	v_lshlrev_b32_e32 v3, 6, v6
	s_movk_i32 s15, 0x3c0
	v_and_or_b32 v2, v3, s15, v2
	v_lshlrev_b32_e32 v3, 2, v6
	s_lshl_b32 s44, s2, 6
	s_lshl_b32 s2, s2, 13
	v_and_b32_e32 v3, 32, v3
	v_bitop3_b32 v4, v2, s2, v3 bitop3:0xde
	s_lshl_b32 s2, s3, 5
	s_and_b32 s45, s2, 0x60
	s_lshl_b32 s2, s45, 7
	s_add_u32 s46, s58, 0x2e000000
	s_addc_u32 s47, s59, 0
	v_bitop3_b32 v2, s2, v2, v3 bitop3:0xf6
	s_add_u32 s2, s8, 0x80
	s_addc_u32 s3, s9, 0
	s_add_i32 s15, s42, 0x18000
	s_waitcnt vmcnt(2)
	s_barrier
	s_mov_b32 m0, s15
	s_nop 0
	global_load_lds_dwordx4 v204, s[2:3]
	s_add_i32 s15, s42, 0x1a000
	s_mov_b32 m0, s15
	s_nop 0
	global_load_lds_dwordx4 v205, s[2:3]
	s_add_u32 s2, s6, 0x80
	s_addc_u32 s3, s7, 0
	s_add_i32 s15, s42, 0x8000
	s_mov_b32 m0, s15
	s_nop 0
	global_load_lds_dwordx4 v66, s[2:3]
	s_add_i32 s15, s42, 0xa000
	s_mov_b32 m0, s15
	s_nop 0
	global_load_lds_dwordx4 v67, s[2:3]
	s_add_u32 s2, s8, 0x2080
	s_addc_u32 s3, s9, 0
	s_add_i32 s15, s42, 0x1c000
	s_mov_b32 m0, s15
	s_nop 0
	global_load_lds_dwordx4 v204, s[2:3]
	s_add_i32 s15, s42, 0x1e000
	s_mov_b32 m0, s15
	s_nop 0
	global_load_lds_dwordx4 v205, s[2:3]
	s_waitcnt vmcnt(6)
	s_cmpk_lt_u32 s14, 0x100
	s_cselect_b64 s[14:15], -1, 0
	s_mov_b32 s16, 0x3c800000
	s_mov_b32 s48, 0xc1c00000
	s_mov_b32 s49, 0xc0e00000
	s_mov_b32 s18, 0xc01d265f
	s_mov_b32 s50, 0x20000
	s_mov_b32 s51, 0x24000
	s_mov_b32 s60, 0x28000
	v_add_u32_e32 v206, 0, v2
	v_add_u32_e32 v207, 0, v4
	v_mov_b32_e32 v208, 0x40e00000
	v_mov_b32_e32 v234, 0x41f80000
	v_mov_b32_e32 v235, 0xc1c00000
	v_mov_b32_e32 v236, 0x41600000
	v_mov_b32_e32 v237, 0xc0c00000
	v_mov_b32_e32 v238, 0x3d042108
	v_mov_b32_e32 v239, 0x3f46318c
	v_mov_b32_e32 v240, 0x3d924925
	v_mov_b32_e32 v241, 0x3f000000
	v_mov_b32_e32 v242, 0x3a042108
	v_mov_b32_e32 v243, 0x3a924925
	s_mov_b64 s[20:21], s[6:7]
	s_barrier
	s_branch .LBB0_957

; __device__ __forceinline__ unsigned pk4_fp8(float a, float b, float c, float d) { int w = __builtin_amdgcn_cvt_pk_fp8_f32(a, b, 0, false); w = __builtin_amdgcn_cvt_pk_fp8_f32(c, d, w, true); return (unsigned)w; }
;     static __device__ __forceinline__ f32x2 act2(f32x2 g, f32x2 u) {
;         g.x = __builtin_amdgcn_fmed3f(g.x, -24.0f, 7.0f); g.y = __builtin_amdgcn_fmed3f(g.y, -24.0f, 7.0f);
;         u.x = __builtin_amdgcn_fmed3f(u.x, -7.0f, 7.0f); u.y = __builtin_amdgcn_fmed3f(u.y, -7.0f, 7.0f);
;         f32x2 z = g * (-1.702f * 1.4426950408889634f);
;         f32x2 d; d.x = __builtin_amdgcn_exp2f(z.x); d.y = __builtin_amdgcn_exp2f(z.y);
;         d = d + 1.0f;
;         const float r = __builtin_amdgcn_rcpf(d.x * d.y);
;         f32x2 sg; sg.x = r * d.y; sg.y = r * d.x;
;         return (u + 1.0f) * (g * sg);
;     }
;     __device__ __forceinline__ void operator()(const f32x4 (&acc)[2][2][4][2], const pg8::Unit& u, int wr, int wc, int fr, int fq) const {
;         const int e = u.aux;
;         unsigned char* Ht = ws + WS_H2 + (size_t)u.pm * TSF8;
;         const int hc = u.pn * 128 + wc * 32 + 8 * fq;
;         const f32x4 bg0 = *(const f32x4*)(bgate + e * FF + hc), bg1 = *(const f32x4*)(bgate + e * FF + hc + 4);
;         const f32x4 bu0 = *(const f32x4*)(bup + e * FF + hc), bu1 = *(const f32x4*)(bup + e * FF + hc + 4);
; #pragma unroll
;         for (int ai = 0; ai < 2; ++ai)
; #pragma unroll
;             for (int m = 0; m < 4; ++m) { const int rl = ai * 128 + wr * 64 + m * 16 + fr;
;                 const f32x4 g0 = acc[ai][0][m][0] * (1.0f / 64.0f) + bg0, g1 = acc[ai][0][m][1] * (1.0f / 64.0f) + bg1, u0 = acc[ai][1][m][0] * (1.0f / 64.0f) + bu0, u1 = acc[ai][1][m][1] * (1.0f / 64.0f) + bu1;
;                 const f32x2 h0 = act2((f32x2){g0[0], g0[1]}, (f32x2){u0[0], u0[1]}), h1 = act2((f32x2){g0[2], g0[3]}, (f32x2){u0[2], u0[3]});
;                 const f32x2 h2 = act2((f32x2){g1[0], g1[1]}, (f32x2){u1[0], u1[1]}), h3 = act2((f32x2){g1[2], g1[3]}, (f32x2){u1[2], u1[3]});
;                 *(u32x2*)(Ht + (size_t)rl * FF + hc) = (u32x2){pk4_fp8(h0.x, h0.y, h1.x, h1.y), pk4_fp8(h2.x, h2.y, h3.x, h3.y)}; }
.Lmy_nobar0:
	v_pk_fma_f32 v[218:219], v[218:219], v[238:239], v[238:239] op_sel:[0,0,1] op_sel_hi:[1,0,1]
	v_pk_fma_f32 v[220:221], v[220:221], v[238:239], v[238:239] op_sel:[0,0,1] op_sel_hi:[1,0,1]
	v_pk_fma_f32 v[222:223], v[222:223], v[238:239], v[238:239] op_sel:[0,0,1] op_sel_hi:[1,0,1]
	v_pk_fma_f32 v[224:225], v[224:225], v[238:239], v[238:239] op_sel:[0,0,1] op_sel_hi:[1,0,1]
	v_pk_fma_f32 v[214:215], v[214:215], v[240:241], v[240:241] op_sel:[0,0,1] op_sel_hi:[1,0,1]
	v_pk_fma_f32 v[216:217], v[216:217], v[240:241], v[240:241] op_sel:[0,0,1] op_sel_hi:[1,0,1]
	v_pk_fma_f32 v[226:227], v[226:227], v[240:241], v[240:241] op_sel:[0,0,1] op_sel_hi:[1,0,1]
	v_pk_fma_f32 v[228:229], v[228:229], v[240:241], v[240:241] op_sel:[0,0,1] op_sel_hi:[1,0,1]
	s_ashr_i32 s23, s22, 31
	s_lshl_b64 s[22:23], s[22:23], 18
	v_mov_b32_e32 v24, v0
	s_add_u32 s22, s46, s22
	s_addc_u32 s23, s47, s23
	s_lshl_b32 s24, s62, 7
	v_lshrrev_b32_e32 v6, 1, v24
	v_and_or_b32 v6, v6, 24, s24
	s_lshl_b32 s24, s61, 10
	s_ashr_i32 s25, s24, 31
	v_or_b32_e32 v22, s45, v6
	s_lshl_b64 s[24:25], s[24:25], 2
	s_add_u32 s26, s84, s24
	v_ashrrev_i32_e32 v23, 31, v22
	s_addc_u32 s27, s85, s25
	v_lshlrev_b64 v[6:7], 2, v[22:23]
	v_lshl_add_u64 v[8:9], s[26:27], 0, v[6:7]
	s_add_u32 s24, s88, s24
	s_addc_u32 s25, s89, s25
	v_lshl_add_u64 v[6:7], s[24:25], 0, v[6:7]
	s_nop 0
	v_and_or_b32 v26, v24, 15, s44
	v_ashrrev_i32_e32 v27, 31, v26
	v_lshlrev_b64 v[32:33], 10, v[26:27]
	v_lshl_add_u64 v[24:25], s[22:23], 0, v[22:23]
	v_lshl_add_u64 v[22:23], v[24:25], 0, v[32:33]
	v_mov_b32_e32 v28, v198
	v_mov_b32_e32 v29, v198
	v_or_b32_e32 v30, 16, v26
	v_pk_fma_f32 v[34:35], v[186:187], v[242:243], v[222:223] op_sel_hi:[1,0,1] clamp
	s_nop 0
	v_pk_fma_f32 v[34:35], v[34:35], v[234:235], v[234:235] op_sel:[0,0,1] op_sel_hi:[1,0,1]
	v_pk_mul_f32 v[56:57], v[34:35], s[18:19] op_sel_hi:[1,0]
	v_pk_fma_f32 v[32:33], v[188:189], v[242:243], v[224:225] op_sel_hi:[1,0,1] clamp
	v_exp_f32_e32 v56, v56
	v_exp_f32_e32 v57, v57
	v_pk_fma_f32 v[38:39], v[194:195], v[242:243], v[218:219] op_sel_hi:[1,0,1] clamp
	v_pk_fma_f32 v[32:33], v[32:33], v[234:235], v[234:235] op_sel:[0,0,1] op_sel_hi:[1,0,1]
	v_pk_fma_f32 v[38:39], v[38:39], v[234:235], v[234:235] op_sel:[0,0,1] op_sel_hi:[1,0,1]
	v_pk_mul_f32 v[58:59], v[32:33], s[18:19] op_sel_hi:[1,0]
	v_pk_mul_f32 v[60:61], v[38:39], s[18:19] op_sel_hi:[1,0]
	v_exp_f32_e32 v58, v58
	v_exp_f32_e32 v59, v59
	v_exp_f32_e32 v60, v60
	v_exp_f32_e32 v61, v61
	v_pk_add_f32 v[56:57], v[56:57], 1.0 op_sel_hi:[1,0]
	v_pk_fma_f32 v[36:37], v[196:197], v[242:243], v[220:221] op_sel_hi:[1,0,1] clamp
	v_mul_f32_e32 v27, v56, v57
	v_pk_fma_f32 v[36:37], v[36:37], v[234:235], v[234:235] op_sel:[0,0,1] op_sel_hi:[1,0,1]
	v_pk_fma_f32 v[64:65], v[172:173], v[242:243], v[228:229] op_sel:[0,1,0] op_sel_hi:[1,1,1] clamp
	v_rcp_f32_e32 v172, v27
	v_pk_mul_f32 v[62:63], v[36:37], s[18:19] op_sel_hi:[1,0]
	v_pk_add_f32 v[58:59], v[58:59], 1.0 op_sel_hi:[1,0]
	v_exp_f32_e32 v62, v62
	v_exp_f32_e32 v63, v63
	v_pk_add_f32 v[60:61], v[60:61], 1.0 op_sel_hi:[1,0]
	v_pk_fma_f32 v[50:51], v[174:175], v[242:243], v[226:227] op_sel:[0,1,0] op_sel_hi:[1,1,1] clamp
	v_mul_f32_e32 v31, v58, v59
	v_mul_f32_e32 v173, v60, v61
	v_pk_fma_f32 v[50:51], v[50:51], v[236:237], v[236:237] op_sel:[0,0,1] op_sel_hi:[1,0,1]
	v_rcp_f32_e32 v174, v31
	v_pk_mul_f32 v[56:57], v[56:57], v[172:173] op_sel:[1,0] op_sel_hi:[0,0]
	v_pk_mul_f32 v[34:35], v[34:35], v[56:57]
	v_pk_add_f32 v[62:63], v[62:63], 1.0 op_sel_hi:[1,0]
	v_pk_mul_f32 v[34:35], v[50:51], v[34:35]
	v_pk_fma_f32 v[48:49], v[176:177], v[242:243], v[228:229] op_sel:[0,1,0] op_sel_hi:[1,1,1] clamp
	v_mul_f32_e32 v175, v62, v63
	v_cvt_pk_fp8_f32 v28, v34, v35
	v_pk_fma_f32 v[48:49], v[48:49], v[236:237], v[236:237] op_sel:[0,0,1] op_sel_hi:[1,0,1]
	v_pk_mul_f32 v[58:59], v[58:59], v[174:175] op_sel:[1,0] op_sel_hi:[0,0]
	v_pk_fma_f32 v[42:43], v[190:191], v[242:243], v[222:223] op_sel_hi:[1,0,1] clamp
	v_rcp_f32_e32 v176, v173
	v_pk_mul_f32 v[32:33], v[32:33], v[58:59]
	v_pk_fma_f32 v[42:43], v[42:43], v[234:235], v[234:235] op_sel:[0,0,1] op_sel_hi:[1,0,1]
	v_pk_mul_f32 v[32:33], v[48:49], v[32:33]
	v_pk_fma_f32 v[54:55], v[178:179], v[242:243], v[214:215] op_sel:[0,1,0] op_sel_hi:[1,1,1] clamp
	v_cvt_pk_fp8_f32 v28, v32, v33 op_sel:[0,0,1]
	v_pk_mul_f32 v[32:33], v[42:43], s[18:19] op_sel_hi:[1,0]
	v_rcp_f32_e32 v178, v175
	v_exp_f32_e32 v32, v32
	v_exp_f32_e32 v33, v33
	v_pk_fma_f32 v[54:55], v[54:55], v[236:237], v[236:237] op_sel:[0,0,1] op_sel_hi:[1,0,1]
	v_pk_mul_f32 v[60:61], v[60:61], v[176:177] op_sel:[1,0] op_sel_hi:[0,0]
	v_pk_mul_f32 v[38:39], v[38:39], v[60:61]
	v_pk_fma_f32 v[40:41], v[192:193], v[242:243], v[224:225] op_sel_hi:[1,0,1] clamp
	v_pk_fma_f32 v[52:53], v[180:181], v[242:243], v[216:217] op_sel:[0,1,0] op_sel_hi:[1,1,1] clamp
	v_pk_mul_f32 v[38:39], v[54:55], v[38:39]
	v_pk_fma_f32 v[52:53], v[52:53], v[236:237], v[236:237] op_sel:[0,0,1] op_sel_hi:[1,0,1]
	v_pk_mul_f32 v[62:63], v[62:63], v[178:179] op_sel:[1,0] op_sel_hi:[0,0]
	v_cvt_pk_fp8_f32 v29, v38, v39
	v_pk_add_f32 v[32:33], v[32:33], 1.0 op_sel_hi:[1,0]
	v_pk_fma_f32 v[38:39], v[40:41], v[234:235], v[234:235] op_sel:[0,0,1] op_sel_hi:[1,0,1]
	v_pk_mul_f32 v[36:37], v[36:37], v[62:63]
	v_mul_f32_e32 v27, v32, v33
	v_pk_mul_f32 v[40:41], v[38:39], s[18:19] op_sel_hi:[1,0]
	v_pk_mul_f32 v[34:35], v[52:53], v[36:37]
	v_rcp_f32_e32 v36, v27
	v_exp_f32_e32 v40, v40
	v_exp_f32_e32 v41, v41
	v_pk_fma_f32 v[46:47], v[182:183], v[242:243], v[218:219] op_sel_hi:[1,0,1] clamp
	v_pk_mul_f32 v[32:33], v[32:33], v[36:37] op_sel:[1,0] op_sel_hi:[0,0]
; __device__ __forceinline__ unsigned pk4_fp8(float a, float b, float c, float d) { int w = __builtin_amdgcn_cvt_pk_fp8_f32(a, b, 0, false); w = __builtin_amdgcn_cvt_pk_fp8_f32(c, d, w, true); return (unsigned)w; }
;     static __device__ __forceinline__ f32x2 act2(f32x2 g, f32x2 u) {
;         g.x = __builtin_amdgcn_fmed3f(g.x, -24.0f, 7.0f); g.y = __builtin_amdgcn_fmed3f(g.y, -24.0f, 7.0f);
;         u.x = __builtin_amdgcn_fmed3f(u.x, -7.0f, 7.0f); u.y = __builtin_amdgcn_fmed3f(u.y, -7.0f, 7.0f);
;         f32x2 z = g * (-1.702f * 1.4426950408889634f);
;         f32x2 d; d.x = __builtin_amdgcn_exp2f(z.x); d.y = __builtin_amdgcn_exp2f(z.y);
;         d = d + 1.0f;
;         const float r = __builtin_amdgcn_rcpf(d.x * d.y);
;         f32x2 sg; sg.x = r * d.y; sg.y = r * d.x;
;         return (u + 1.0f) * (g * sg);
;     }
;     __device__ __forceinline__ void operator()(const f32x4 (&acc)[2][2][4][2], const pg8::Unit& u, int wr, int wc, int fr, int fq) const {
;         const int e = u.aux;
;         unsigned char* Ht = ws + WS_H2 + (size_t)u.pm * TSF8;
;         const int hc = u.pn * 128 + wc * 32 + 8 * fq;
;         const f32x4 bg0 = *(const f32x4*)(bgate + e * FF + hc), bg1 = *(const f32x4*)(bgate + e * FF + hc + 4);
;         const f32x4 bu0 = *(const f32x4*)(bup + e * FF + hc), bu1 = *(const f32x4*)(bup + e * FF + hc + 4);
; #pragma unroll
;         for (int ai = 0; ai < 2; ++ai)
; #pragma unroll
;             for (int m = 0; m < 4; ++m) { const int rl = ai * 128 + wr * 64 + m * 16 + fr;
;                 const f32x4 g0 = acc[ai][0][m][0] * (1.0f / 64.0f) + bg0, g1 = acc[ai][0][m][1] * (1.0f / 64.0f) + bg1, u0 = acc[ai][1][m][0] * (1.0f / 64.0f) + bu0, u1 = acc[ai][1][m][1] * (1.0f / 64.0f) + bu1;
;                 const f32x2 h0 = act2((f32x2){g0[0], g0[1]}, (f32x2){u0[0], u0[1]}), h1 = act2((f32x2){g0[2], g0[3]}, (f32x2){u0[2], u0[3]});
;                 const f32x2 h2 = act2((f32x2){g1[0], g1[1]}, (f32x2){u1[0], u1[1]}), h3 = act2((f32x2){g1[2], g1[3]}, (f32x2){u1[2], u1[3]});
;                 *(u32x2*)(Ht + (size_t)rl * FF + hc) = (u32x2){pk4_fp8(h0.x, h0.y, h1.x, h1.y), pk4_fp8(h2.x, h2.y, h3.x, h3.y)}; }
	v_pk_fma_f32 v[170:171], v[170:171], v[242:243], v[226:227] op_sel:[0,1,0] op_sel_hi:[1,1,1] clamp
	v_pk_add_f32 v[36:37], v[40:41], 1.0 op_sel_hi:[1,0]
	v_cvt_pk_fp8_f32 v29, v34, v35 op_sel:[0,0,1]
	v_mul_f32_e32 v27, v36, v37
	v_rcp_f32_e32 v40, v27
	v_pk_fma_f32 v[34:35], v[170:171], v[236:237], v[236:237] op_sel:[0,0,1] op_sel_hi:[1,0,1]
	v_pk_mul_f32 v[36:37], v[36:37], v[40:41] op_sel:[1,0] op_sel_hi:[0,0]
	v_pk_mul_f32 v[36:37], v[38:39], v[36:37]
	v_pk_fma_f32 v[38:39], v[46:47], v[234:235], v[234:235] op_sel:[0,0,1] op_sel_hi:[1,0,1]
	v_pk_mul_f32 v[40:41], v[38:39], s[18:19] op_sel_hi:[1,0]
	v_pk_mul_f32 v[32:33], v[42:43], v[32:33]
	v_exp_f32_e32 v40, v40
	v_exp_f32_e32 v41, v41
	v_pk_mul_f32 v[32:33], v[34:35], v[32:33]
	v_pk_fma_f32 v[34:35], v[64:65], v[236:237], v[236:237] op_sel:[0,0,1] op_sel_hi:[1,0,1]
	v_pk_fma_f32 v[44:45], v[184:185], v[242:243], v[220:221] op_sel_hi:[1,0,1] clamp
	v_pk_mul_f32 v[34:35], v[34:35], v[36:37]
	v_pk_add_f32 v[36:37], v[40:41], 1.0 op_sel_hi:[1,0]
	v_pk_fma_f32 v[42:43], v[44:45], v[234:235], v[234:235] op_sel:[0,0,1] op_sel_hi:[1,0,1]
	v_mul_f32_e32 v27, v36, v37
	v_rcp_f32_e32 v40, v27
	v_pk_mul_f32 v[44:45], v[42:43], s[18:19] op_sel_hi:[1,0]
	global_store_dwordx2 v[22:23], v[28:29], off
	v_exp_f32_e32 v44, v44
	v_exp_f32_e32 v45, v45
	v_pk_mul_f32 v[36:37], v[36:37], v[40:41] op_sel:[1,0] op_sel_hi:[0,0]
	v_pk_mul_f32 v[36:37], v[38:39], v[36:37]
	v_pk_fma_f32 v[28:29], v[166:167], v[242:243], v[214:215] op_sel:[0,1,0] op_sel_hi:[1,1,1] clamp
	v_pk_add_f32 v[38:39], v[44:45], 1.0 op_sel_hi:[1,0]
	v_pk_fma_f32 v[28:29], v[28:29], v[236:237], v[236:237] op_sel:[0,0,1] op_sel_hi:[1,0,1]
	v_mul_f32_e32 v27, v38, v39
	v_rcp_f32_e32 v40, v27
	v_pk_fma_f32 v[168:169], v[168:169], v[242:243], v[216:217] op_sel:[0,1,0] op_sel_hi:[1,1,1] clamp
	v_pk_mul_f32 v[38:39], v[38:39], v[40:41] op_sel:[1,0] op_sel_hi:[0,0]
	v_mov_b32_e32 v40, v198
	v_cvt_pk_fp8_f32 v40, v32, v33
	v_pk_fma_f32 v[32:33], v[154:155], v[242:243], v[222:223] op_sel_hi:[1,0,1] clamp
	v_pk_mul_f32 v[28:29], v[28:29], v[36:37]
	v_pk_fma_f32 v[32:33], v[32:33], v[234:235], v[234:235] op_sel:[0,0,1] op_sel_hi:[1,0,1]
	v_mov_b32_e32 v41, v198
	v_pk_mul_f32 v[44:45], v[32:33], s[18:19] op_sel_hi:[1,0]
	v_cvt_pk_fp8_f32 v41, v28, v29
	v_exp_f32_e32 v44, v44
	v_exp_f32_e32 v45, v45
	v_pk_fma_f32 v[36:37], v[168:169], v[236:237], v[236:237] op_sel:[0,0,1] op_sel_hi:[1,0,1]
	v_pk_mul_f32 v[28:29], v[42:43], v[38:39]
	v_ashrrev_i32_e32 v31, 31, v30
	v_pk_mul_f32 v[28:29], v[36:37], v[28:29]
	v_pk_add_f32 v[44:45], v[44:45], 1.0 op_sel_hi:[1,0]
	v_cvt_pk_fp8_f32 v41, v28, v29 op_sel:[0,0,1]
	v_lshlrev_b64 v[28:29], 10, v[30:31]
	v_pk_fma_f32 v[30:31], v[156:157], v[242:243], v[224:225] op_sel_hi:[1,0,1] clamp
	v_mul_f32_e32 v27, v44, v45
	v_pk_fma_f32 v[30:31], v[30:31], v[234:235], v[234:235] op_sel:[0,0,1] op_sel_hi:[1,0,1]
	v_rcp_f32_e32 v48, v27
	v_pk_mul_f32 v[50:51], v[30:31], s[18:19] op_sel_hi:[1,0]
	v_cvt_pk_fp8_f32 v40, v34, v35 op_sel:[0,0,1]
	v_exp_f32_e32 v50, v50
	v_exp_f32_e32 v51, v51
	v_pk_mul_f32 v[44:45], v[44:45], v[48:49] op_sel:[1,0] op_sel_hi:[0,0]
	v_pk_mul_f32 v[32:33], v[32:33], v[44:45]
	v_lshl_add_u64 v[28:29], v[24:25], 0, v[28:29]
	v_pk_add_f32 v[44:45], v[50:51], 1.0 op_sel_hi:[1,0]
	global_store_dwordx2 v[28:29], v[40:41], off
	v_mul_f32_e32 v27, v44, v45
	v_rcp_f32_e32 v48, v27
	v_pk_fma_f32 v[40:41], v[162:163], v[242:243], v[226:227] op_sel:[0,1,0] op_sel_hi:[1,1,1] clamp
	v_pk_fma_f32 v[36:37], v[150:151], v[242:243], v[218:219] op_sel_hi:[1,0,1] clamp
	v_pk_fma_f32 v[40:41], v[40:41], v[236:237], v[236:237] op_sel:[0,0,1] op_sel_hi:[1,0,1]
	v_pk_fma_f32 v[36:37], v[36:37], v[234:235], v[234:235] op_sel:[0,0,1] op_sel_hi:[1,0,1]
	v_pk_mul_f32 v[32:33], v[40:41], v[32:33]
	v_pk_mul_f32 v[40:41], v[44:45], v[48:49] op_sel:[1,0] op_sel_hi:[0,0]
	v_pk_mul_f32 v[30:31], v[30:31], v[40:41]
	v_pk_mul_f32 v[40:41], v[36:37], s[18:19] op_sel_hi:[1,0]
	v_pk_fma_f32 v[38:39], v[164:165], v[242:243], v[228:229] op_sel:[0,1,0] op_sel_hi:[1,1,1] clamp
	v_exp_f32_e32 v40, v40
	v_exp_f32_e32 v41, v41
	v_pk_fma_f32 v[34:35], v[152:153], v[242:243], v[220:221] op_sel_hi:[1,0,1] clamp
	v_pk_fma_f32 v[38:39], v[38:39], v[236:237], v[236:237] op_sel:[0,0,1] op_sel_hi:[1,0,1]
	v_pk_add_f32 v[40:41], v[40:41], 1.0 op_sel_hi:[1,0]
	v_pk_fma_f32 v[46:47], v[158:159], v[242:243], v[214:215] op_sel:[0,1,0] op_sel_hi:[1,1,1] clamp
	v_mul_f32_e32 v27, v40, v41
	v_pk_fma_f32 v[34:35], v[34:35], v[234:235], v[234:235] op_sel:[0,0,1] op_sel_hi:[1,0,1]
	v_pk_mul_f32 v[30:31], v[38:39], v[30:31]
	v_pk_fma_f32 v[38:39], v[46:47], v[236:237], v[236:237] op_sel:[0,0,1] op_sel_hi:[1,0,1]
	v_rcp_f32_e32 v44, v27
	v_pk_mul_f32 v[46:47], v[34:35], s[18:19] op_sel_hi:[1,0]
	v_pk_fma_f32 v[42:43], v[160:161], v[242:243], v[216:217] op_sel:[0,1,0] op_sel_hi:[1,1,1] clamp
	v_exp_f32_e32 v46, v46
	v_exp_f32_e32 v47, v47
	v_pk_mul_f32 v[40:41], v[40:41], v[44:45] op_sel:[1,0] op_sel_hi:[0,0]
	v_pk_mul_f32 v[36:37], v[36:37], v[40:41]
	v_pk_add_f32 v[40:41], v[46:47], 1.0 op_sel_hi:[1,0]
	v_pk_mul_f32 v[36:37], v[38:39], v[36:37]
	v_mul_f32_e32 v27, v40, v41
	v_rcp_f32_e32 v44, v27
	v_pk_fma_f32 v[38:39], v[42:43], v[236:237], v[236:237] op_sel:[0,0,1] op_sel_hi:[1,0,1]
	v_mov_b32_e32 v42, v198
	v_mov_b32_e32 v43, v198
	v_cvt_pk_fp8_f32 v42, v32, v33
	v_cvt_pk_fp8_f32 v43, v36, v37
	v_pk_mul_f32 v[40:41], v[40:41], v[44:45] op_sel:[1,0] op_sel_hi:[0,0]
	v_pk_mul_f32 v[32:33], v[34:35], v[40:41]
	v_or_b32_e32 v28, 32, v26
	v_pk_mul_f32 v[32:33], v[38:39], v[32:33]
	v_cvt_pk_fp8_f32 v42, v30, v31 op_sel:[0,0,1]
	v_cvt_pk_fp8_f32 v43, v32, v33 op_sel:[0,0,1]
; __device__ __forceinline__ unsigned pk4_fp8(float a, float b, float c, float d) { int w = __builtin_amdgcn_cvt_pk_fp8_f32(a, b, 0, false); w = __builtin_amdgcn_cvt_pk_fp8_f32(c, d, w, true); return (unsigned)w; }
;     static __device__ __forceinline__ f32x2 act2(f32x2 g, f32x2 u) {
;         g.x = __builtin_amdgcn_fmed3f(g.x, -24.0f, 7.0f); g.y = __builtin_amdgcn_fmed3f(g.y, -24.0f, 7.0f);
;         u.x = __builtin_amdgcn_fmed3f(u.x, -7.0f, 7.0f); u.y = __builtin_amdgcn_fmed3f(u.y, -7.0f, 7.0f);
;         f32x2 z = g * (-1.702f * 1.4426950408889634f);
;         f32x2 d; d.x = __builtin_amdgcn_exp2f(z.x); d.y = __builtin_amdgcn_exp2f(z.y);
;         d = d + 1.0f;
;         const float r = __builtin_amdgcn_rcpf(d.x * d.y);
;         f32x2 sg; sg.x = r * d.y; sg.y = r * d.x;
;         return (u + 1.0f) * (g * sg);
;     }
;     __device__ __forceinline__ void operator()(const f32x4 (&acc)[2][2][4][2], const pg8::Unit& u, int wr, int wc, int fr, int fq) const {
;         const int e = u.aux;
;         unsigned char* Ht = ws + WS_H2 + (size_t)u.pm * TSF8;
;         const int hc = u.pn * 128 + wc * 32 + 8 * fq;
;         const f32x4 bg0 = *(const f32x4*)(bgate + e * FF + hc), bg1 = *(const f32x4*)(bgate + e * FF + hc + 4);
;         const f32x4 bu0 = *(const f32x4*)(bup + e * FF + hc), bu1 = *(const f32x4*)(bup + e * FF + hc + 4);
; #pragma unroll
;         for (int ai = 0; ai < 2; ++ai)
; #pragma unroll
;             for (int m = 0; m < 4; ++m) { const int rl = ai * 128 + wr * 64 + m * 16 + fr;
;                 const f32x4 g0 = acc[ai][0][m][0] * (1.0f / 64.0f) + bg0, g1 = acc[ai][0][m][1] * (1.0f / 64.0f) + bg1, u0 = acc[ai][1][m][0] * (1.0f / 64.0f) + bu0, u1 = acc[ai][1][m][1] * (1.0f / 64.0f) + bu1;
;                 const f32x2 h0 = act2((f32x2){g0[0], g0[1]}, (f32x2){u0[0], u0[1]}), h1 = act2((f32x2){g0[2], g0[3]}, (f32x2){u0[2], u0[3]});
;                 const f32x2 h2 = act2((f32x2){g1[0], g1[1]}, (f32x2){u1[0], u1[1]}), h3 = act2((f32x2){g1[2], g1[3]}, (f32x2){u1[2], u1[3]});
;                 *(u32x2*)(Ht + (size_t)rl * FF + hc) = (u32x2){pk4_fp8(h0.x, h0.y, h1.x, h1.y), pk4_fp8(h2.x, h2.y, h3.x, h3.y)}; }
	v_ashrrev_i32_e32 v29, 31, v28
	v_lshlrev_b64 v[28:29], 10, v[28:29]
	v_pk_fma_f32 v[30:31], v[138:139], v[242:243], v[222:223] op_sel_hi:[1,0,1] clamp
	v_lshl_add_u64 v[28:29], v[24:25], 0, v[28:29]
	v_pk_fma_f32 v[30:31], v[30:31], v[234:235], v[234:235] op_sel:[0,0,1] op_sel_hi:[1,0,1]
	global_store_dwordx2 v[28:29], v[42:43], off
	v_pk_mul_f32 v[42:43], v[30:31], s[18:19] op_sel_hi:[1,0]
	v_pk_fma_f32 v[28:29], v[140:141], v[242:243], v[224:225] op_sel_hi:[1,0,1] clamp
	v_exp_f32_e32 v42, v42
	v_exp_f32_e32 v43, v43
	v_pk_fma_f32 v[28:29], v[28:29], v[234:235], v[234:235] op_sel:[0,0,1] op_sel_hi:[1,0,1]
	v_pk_mul_f32 v[48:49], v[28:29], s[18:19] op_sel_hi:[1,0]
	v_pk_add_f32 v[42:43], v[42:43], 1.0 op_sel_hi:[1,0]
	v_exp_f32_e32 v48, v48
	v_mul_f32_e32 v27, v42, v43
	v_rcp_f32_e32 v46, v27
	v_exp_f32_e32 v49, v49
	v_pk_fma_f32 v[38:39], v[146:147], v[242:243], v[226:227] op_sel:[0,1,0] op_sel_hi:[1,1,1] clamp
	v_pk_fma_f32 v[34:35], v[134:135], v[242:243], v[218:219] op_sel_hi:[1,0,1] clamp
	v_pk_mul_f32 v[42:43], v[42:43], v[46:47] op_sel:[1,0] op_sel_hi:[0,0]
	v_pk_mul_f32 v[30:31], v[30:31], v[42:43]
	v_pk_add_f32 v[42:43], v[48:49], 1.0 op_sel_hi:[1,0]
	v_pk_fma_f32 v[38:39], v[38:39], v[236:237], v[236:237] op_sel:[0,0,1] op_sel_hi:[1,0,1]
	v_mul_f32_e32 v27, v42, v43
	v_rcp_f32_e32 v46, v27
	v_pk_fma_f32 v[34:35], v[34:35], v[234:235], v[234:235] op_sel:[0,0,1] op_sel_hi:[1,0,1]
	v_pk_mul_f32 v[30:31], v[38:39], v[30:31]
	v_pk_mul_f32 v[38:39], v[42:43], v[46:47] op_sel:[1,0] op_sel_hi:[0,0]
	v_pk_mul_f32 v[28:29], v[28:29], v[38:39]
	v_pk_mul_f32 v[38:39], v[34:35], s[18:19] op_sel_hi:[1,0]
	v_pk_fma_f32 v[36:37], v[148:149], v[242:243], v[228:229] op_sel:[0,1,0] op_sel_hi:[1,1,1] clamp
	v_exp_f32_e32 v38, v38
	v_exp_f32_e32 v39, v39
	v_pk_fma_f32 v[32:33], v[136:137], v[242:243], v[220:221] op_sel_hi:[1,0,1] clamp
	v_pk_fma_f32 v[36:37], v[36:37], v[236:237], v[236:237] op_sel:[0,0,1] op_sel_hi:[1,0,1]
	v_pk_add_f32 v[38:39], v[38:39], 1.0 op_sel_hi:[1,0]
	v_pk_fma_f32 v[44:45], v[142:143], v[242:243], v[214:215] op_sel:[0,1,0] op_sel_hi:[1,1,1] clamp
	v_mul_f32_e32 v27, v38, v39
	v_pk_fma_f32 v[32:33], v[32:33], v[234:235], v[234:235] op_sel:[0,0,1] op_sel_hi:[1,0,1]
	v_pk_mul_f32 v[28:29], v[36:37], v[28:29]
	v_pk_fma_f32 v[36:37], v[44:45], v[236:237], v[236:237] op_sel:[0,0,1] op_sel_hi:[1,0,1]
	v_rcp_f32_e32 v42, v27
	v_pk_mul_f32 v[44:45], v[32:33], s[18:19] op_sel_hi:[1,0]
	v_or_b32_e32 v26, 48, v26
	v_exp_f32_e32 v44, v44
	v_exp_f32_e32 v45, v45
	v_pk_mul_f32 v[38:39], v[38:39], v[42:43] op_sel:[1,0] op_sel_hi:[0,0]
	v_pk_mul_f32 v[34:35], v[34:35], v[38:39]
	v_pk_fma_f32 v[40:41], v[144:145], v[242:243], v[216:217] op_sel:[0,1,0] op_sel_hi:[1,1,1] clamp
	v_pk_add_f32 v[38:39], v[44:45], 1.0 op_sel_hi:[1,0]
	v_mul_f32_e32 v27, v38, v39
	v_rcp_f32_e32 v42, v27
	v_pk_mul_f32 v[34:35], v[36:37], v[34:35]
	v_pk_fma_f32 v[36:37], v[40:41], v[236:237], v[236:237] op_sel:[0,0,1] op_sel_hi:[1,0,1]
	v_mov_b32_e32 v40, v198
	v_mov_b32_e32 v41, v198
	v_ashrrev_i32_e32 v27, 31, v26
	v_cvt_pk_fp8_f32 v40, v30, v31
	v_cvt_pk_fp8_f32 v41, v34, v35
	v_lshlrev_b64 v[26:27], 10, v[26:27]
	v_pk_mul_f32 v[38:39], v[38:39], v[42:43] op_sel:[1,0] op_sel_hi:[0,0]
	v_lshl_add_u64 v[24:25], v[24:25], 0, v[26:27]
	v_pk_fma_f32 v[26:27], v[122:123], v[242:243], v[222:223] op_sel_hi:[1,0,1] clamp
	v_pk_mul_f32 v[30:31], v[32:33], v[38:39]
	v_pk_fma_f32 v[26:27], v[26:27], v[234:235], v[234:235] op_sel:[0,0,1] op_sel_hi:[1,0,1]
	v_pk_mul_f32 v[30:31], v[36:37], v[30:31]
	v_pk_mul_f32 v[38:39], v[26:27], s[18:19] op_sel_hi:[1,0]
	v_cvt_pk_fp8_f32 v40, v28, v29 op_sel:[0,0,1]
	v_cvt_pk_fp8_f32 v41, v30, v31 op_sel:[0,0,1]
	v_exp_f32_e32 v38, v38
	v_exp_f32_e32 v39, v39
	v_pk_fma_f32 v[34:35], v[130:131], v[242:243], v[226:227] op_sel:[0,1,0] op_sel_hi:[1,1,1] clamp
	global_store_dwordx2 v[24:25], v[40:41], off
	v_pk_fma_f32 v[24:25], v[124:125], v[242:243], v[224:225] op_sel_hi:[1,0,1] clamp
	v_pk_add_f32 v[38:39], v[38:39], 1.0 op_sel_hi:[1,0]
	v_pk_fma_f32 v[24:25], v[24:25], v[234:235], v[234:235] op_sel:[0,0,1] op_sel_hi:[1,0,1]
	v_mul_f32_e32 v42, v38, v39
	v_rcp_f32_e32 v42, v42
	v_pk_mul_f32 v[44:45], v[24:25], s[18:19] op_sel_hi:[1,0]
	v_pk_fma_f32 v[34:35], v[34:35], v[236:237], v[236:237] op_sel:[0,0,1] op_sel_hi:[1,0,1]
	v_exp_f32_e32 v44, v44
	v_exp_f32_e32 v45, v45
	v_pk_mul_f32 v[38:39], v[38:39], v[42:43] op_sel:[1,0] op_sel_hi:[0,0]
	v_pk_mul_f32 v[26:27], v[26:27], v[38:39]
	v_pk_add_f32 v[38:39], v[44:45], 1.0 op_sel_hi:[1,0]
	v_pk_fma_f32 v[30:31], v[118:119], v[242:243], v[218:219] op_sel_hi:[1,0,1] clamp
	v_mul_f32_e32 v42, v38, v39
	v_rcp_f32_e32 v42, v42
	v_pk_fma_f32 v[30:31], v[30:31], v[234:235], v[234:235] op_sel:[0,0,1] op_sel_hi:[1,0,1]
	v_pk_mul_f32 v[26:27], v[34:35], v[26:27]
	v_pk_mul_f32 v[34:35], v[38:39], v[42:43] op_sel:[1,0] op_sel_hi:[0,0]
	v_pk_mul_f32 v[24:25], v[24:25], v[34:35]
	v_pk_mul_f32 v[34:35], v[30:31], s[18:19] op_sel_hi:[1,0]
	v_pk_fma_f32 v[32:33], v[132:133], v[242:243], v[228:229] op_sel:[0,1,0] op_sel_hi:[1,1,1] clamp
	v_exp_f32_e32 v34, v34
	v_exp_f32_e32 v35, v35
	v_pk_fma_f32 v[28:29], v[120:121], v[242:243], v[220:221] op_sel_hi:[1,0,1] clamp
	v_pk_fma_f32 v[32:33], v[32:33], v[236:237], v[236:237] op_sel:[0,0,1] op_sel_hi:[1,0,1]
	v_pk_add_f32 v[34:35], v[34:35], 1.0 op_sel_hi:[1,0]
	v_pk_fma_f32 v[40:41], v[126:127], v[242:243], v[214:215] op_sel:[0,1,0] op_sel_hi:[1,1,1] clamp
	v_mul_f32_e32 v38, v34, v35
	v_pk_fma_f32 v[28:29], v[28:29], v[234:235], v[234:235] op_sel:[0,0,1] op_sel_hi:[1,0,1]
	v_pk_mul_f32 v[24:25], v[32:33], v[24:25]
; __device__ __forceinline__ unsigned pk4_fp8(float a, float b, float c, float d) { int w = __builtin_amdgcn_cvt_pk_fp8_f32(a, b, 0, false); w = __builtin_amdgcn_cvt_pk_fp8_f32(c, d, w, true); return (unsigned)w; }
;     static __device__ __forceinline__ f32x2 act2(f32x2 g, f32x2 u) {
;         g.x = __builtin_amdgcn_fmed3f(g.x, -24.0f, 7.0f); g.y = __builtin_amdgcn_fmed3f(g.y, -24.0f, 7.0f);
;         u.x = __builtin_amdgcn_fmed3f(u.x, -7.0f, 7.0f); u.y = __builtin_amdgcn_fmed3f(u.y, -7.0f, 7.0f);
;         f32x2 z = g * (-1.702f * 1.4426950408889634f);
;         f32x2 d; d.x = __builtin_amdgcn_exp2f(z.x); d.y = __builtin_amdgcn_exp2f(z.y);
;         d = d + 1.0f;
;         const float r = __builtin_amdgcn_rcpf(d.x * d.y);
;         f32x2 sg; sg.x = r * d.y; sg.y = r * d.x;
;         return (u + 1.0f) * (g * sg);
;     }
;     __device__ __forceinline__ void operator()(const f32x4 (&acc)[2][2][4][2], const pg8::Unit& u, int wr, int wc, int fr, int fq) const {
;         const int e = u.aux;
;         unsigned char* Ht = ws + WS_H2 + (size_t)u.pm * TSF8;
;         const int hc = u.pn * 128 + wc * 32 + 8 * fq;
;         const f32x4 bg0 = *(const f32x4*)(bgate + e * FF + hc), bg1 = *(const f32x4*)(bgate + e * FF + hc + 4);
;         const f32x4 bu0 = *(const f32x4*)(bup + e * FF + hc), bu1 = *(const f32x4*)(bup + e * FF + hc + 4);
; #pragma unroll
;         for (int ai = 0; ai < 2; ++ai)
; #pragma unroll
;             for (int m = 0; m < 4; ++m) { const int rl = ai * 128 + wr * 64 + m * 16 + fr;
;                 const f32x4 g0 = acc[ai][0][m][0] * (1.0f / 64.0f) + bg0, g1 = acc[ai][0][m][1] * (1.0f / 64.0f) + bg1, u0 = acc[ai][1][m][0] * (1.0f / 64.0f) + bu0, u1 = acc[ai][1][m][1] * (1.0f / 64.0f) + bu1;
;                 const f32x2 h0 = act2((f32x2){g0[0], g0[1]}, (f32x2){u0[0], u0[1]}), h1 = act2((f32x2){g0[2], g0[3]}, (f32x2){u0[2], u0[3]});
;                 const f32x2 h2 = act2((f32x2){g1[0], g1[1]}, (f32x2){u1[0], u1[1]}), h3 = act2((f32x2){g1[2], g1[3]}, (f32x2){u1[2], u1[3]});
;                 *(u32x2*)(Ht + (size_t)rl * FF + hc) = (u32x2){pk4_fp8(h0.x, h0.y, h1.x, h1.y), pk4_fp8(h2.x, h2.y, h3.x, h3.y)}; }
	v_pk_fma_f32 v[32:33], v[40:41], v[236:237], v[236:237] op_sel:[0,0,1] op_sel_hi:[1,0,1]
	v_rcp_f32_e32 v38, v38
	v_pk_mul_f32 v[40:41], v[28:29], s[18:19] op_sel_hi:[1,0]
	v_pk_fma_f32 v[36:37], v[128:129], v[242:243], v[216:217] op_sel:[0,1,0] op_sel_hi:[1,1,1] clamp
	v_exp_f32_e32 v40, v40
	v_exp_f32_e32 v41, v41
	v_pk_mul_f32 v[34:35], v[34:35], v[38:39] op_sel:[1,0] op_sel_hi:[0,0]
	v_pk_mul_f32 v[30:31], v[30:31], v[34:35]
	v_pk_add_f32 v[34:35], v[40:41], 1.0 op_sel_hi:[1,0]
	v_pk_mul_f32 v[30:31], v[32:33], v[30:31]
	v_mul_f32_e32 v38, v34, v35
	v_rcp_f32_e32 v38, v38
	v_pk_fma_f32 v[32:33], v[36:37], v[236:237], v[236:237] op_sel:[0,0,1] op_sel_hi:[1,0,1]
	v_mov_b32_e32 v37, v198
	v_cvt_pk_fp8_f32 v37, v30, v31
	v_pk_mul_f32 v[34:35], v[34:35], v[38:39] op_sel:[1,0] op_sel_hi:[0,0]
	v_mov_b32_e32 v36, v198
	v_cvt_pk_fp8_f32 v36, v26, v27
	v_pk_mul_f32 v[26:27], v[28:29], v[34:35]
	v_pk_fma_f32 v[34:35], v[114:115], v[242:243], v[226:227] op_sel:[0,1,0] op_sel_hi:[1,1,1] clamp
	v_pk_mul_f32 v[26:27], v[32:33], v[26:27]
	v_cvt_pk_fp8_f32 v36, v24, v25 op_sel:[0,0,1]
	v_cvt_pk_fp8_f32 v37, v26, v27 op_sel:[0,0,1]
	v_pk_fma_f32 v[26:27], v[106:107], v[242:243], v[222:223] op_sel_hi:[1,0,1] clamp
	v_add_co_u32_e32 v24, vcc, s50, v22
	v_pk_fma_f32 v[26:27], v[26:27], v[234:235], v[234:235] op_sel:[0,0,1] op_sel_hi:[1,0,1]
	v_pk_mul_f32 v[38:39], v[26:27], s[18:19] op_sel_hi:[1,0]
	v_addc_co_u32_e32 v25, vcc, 0, v23, vcc
	v_exp_f32_e32 v38, v38
	v_exp_f32_e32 v39, v39
	global_store_dwordx2 v[24:25], v[36:37], off
	v_pk_fma_f32 v[24:25], v[108:109], v[242:243], v[224:225] op_sel_hi:[1,0,1] clamp
	v_pk_fma_f32 v[34:35], v[34:35], v[236:237], v[236:237] op_sel:[0,0,1] op_sel_hi:[1,0,1]
	v_pk_add_f32 v[38:39], v[38:39], 1.0 op_sel_hi:[1,0]
	v_pk_fma_f32 v[24:25], v[24:25], v[234:235], v[234:235] op_sel:[0,0,1] op_sel_hi:[1,0,1]
	v_mul_f32_e32 v42, v38, v39
	v_rcp_f32_e32 v42, v42
	v_pk_mul_f32 v[44:45], v[24:25], s[18:19] op_sel_hi:[1,0]
	v_exp_f32_e32 v44, v44
	v_exp_f32_e32 v45, v45
	v_pk_mul_f32 v[38:39], v[38:39], v[42:43] op_sel:[1,0] op_sel_hi:[0,0]
	v_pk_mul_f32 v[26:27], v[26:27], v[38:39]
	v_pk_fma_f32 v[30:31], v[102:103], v[242:243], v[218:219] op_sel_hi:[1,0,1] clamp
	v_pk_add_f32 v[38:39], v[44:45], 1.0 op_sel_hi:[1,0]
	v_mul_f32_e32 v42, v38, v39
	v_rcp_f32_e32 v42, v42
	v_pk_mul_f32 v[26:27], v[34:35], v[26:27]
	v_pk_fma_f32 v[30:31], v[30:31], v[234:235], v[234:235] op_sel:[0,0,1] op_sel_hi:[1,0,1]
	v_pk_mul_f32 v[34:35], v[38:39], v[42:43] op_sel:[1,0] op_sel_hi:[0,0]
	v_pk_mul_f32 v[24:25], v[24:25], v[34:35]
	v_pk_mul_f32 v[34:35], v[30:31], s[18:19] op_sel_hi:[1,0]
	v_pk_fma_f32 v[32:33], v[116:117], v[242:243], v[228:229] op_sel:[0,1,0] op_sel_hi:[1,1,1] clamp
	v_exp_f32_e32 v34, v34
	v_exp_f32_e32 v35, v35
	v_pk_fma_f32 v[28:29], v[104:105], v[242:243], v[220:221] op_sel_hi:[1,0,1] clamp
	v_pk_fma_f32 v[32:33], v[32:33], v[236:237], v[236:237] op_sel:[0,0,1] op_sel_hi:[1,0,1]
	v_pk_add_f32 v[34:35], v[34:35], 1.0 op_sel_hi:[1,0]
	v_pk_fma_f32 v[40:41], v[110:111], v[242:243], v[214:215] op_sel:[0,1,0] op_sel_hi:[1,1,1] clamp
	v_mul_f32_e32 v38, v34, v35
	v_pk_fma_f32 v[28:29], v[28:29], v[234:235], v[234:235] op_sel:[0,0,1] op_sel_hi:[1,0,1]
	v_pk_mul_f32 v[24:25], v[32:33], v[24:25]
	v_pk_fma_f32 v[32:33], v[40:41], v[236:237], v[236:237] op_sel:[0,0,1] op_sel_hi:[1,0,1]
	v_rcp_f32_e32 v38, v38
	v_pk_mul_f32 v[40:41], v[28:29], s[18:19] op_sel_hi:[1,0]
	v_pk_fma_f32 v[36:37], v[112:113], v[242:243], v[216:217] op_sel:[0,1,0] op_sel_hi:[1,1,1] clamp
	v_exp_f32_e32 v40, v40
	v_exp_f32_e32 v41, v41
	v_pk_mul_f32 v[34:35], v[34:35], v[38:39] op_sel:[1,0] op_sel_hi:[0,0]
	v_pk_mul_f32 v[30:31], v[30:31], v[34:35]
	v_pk_add_f32 v[34:35], v[40:41], 1.0 op_sel_hi:[1,0]
	v_pk_mul_f32 v[30:31], v[32:33], v[30:31]
	v_mul_f32_e32 v38, v34, v35
	v_rcp_f32_e32 v38, v38
	v_pk_fma_f32 v[32:33], v[36:37], v[236:237], v[236:237] op_sel:[0,0,1] op_sel_hi:[1,0,1]
	v_mov_b32_e32 v37, v198
	v_cvt_pk_fp8_f32 v37, v30, v31
	v_pk_mul_f32 v[34:35], v[34:35], v[38:39] op_sel:[1,0] op_sel_hi:[0,0]
	v_mov_b32_e32 v36, v198
	v_cvt_pk_fp8_f32 v36, v26, v27
	v_pk_mul_f32 v[26:27], v[28:29], v[34:35]
	v_pk_fma_f32 v[34:35], v[98:99], v[242:243], v[226:227] op_sel:[0,1,0] op_sel_hi:[1,1,1] clamp
	v_pk_mul_f32 v[26:27], v[32:33], v[26:27]
	v_cvt_pk_fp8_f32 v36, v24, v25 op_sel:[0,0,1]
	v_cvt_pk_fp8_f32 v37, v26, v27 op_sel:[0,0,1]
	v_pk_fma_f32 v[26:27], v[90:91], v[242:243], v[222:223] op_sel_hi:[1,0,1] clamp
	v_add_co_u32_e32 v24, vcc, s51, v22
	v_pk_fma_f32 v[26:27], v[26:27], v[234:235], v[234:235] op_sel:[0,0,1] op_sel_hi:[1,0,1]
	v_pk_mul_f32 v[38:39], v[26:27], s[18:19] op_sel_hi:[1,0]
	v_addc_co_u32_e32 v25, vcc, 0, v23, vcc
	v_exp_f32_e32 v38, v38
	v_exp_f32_e32 v39, v39
	global_store_dwordx2 v[24:25], v[36:37], off
	v_pk_fma_f32 v[24:25], v[92:93], v[242:243], v[224:225] op_sel_hi:[1,0,1] clamp
	v_pk_fma_f32 v[34:35], v[34:35], v[236:237], v[236:237] op_sel:[0,0,1] op_sel_hi:[1,0,1]
	v_pk_add_f32 v[38:39], v[38:39], 1.0 op_sel_hi:[1,0]
	v_pk_fma_f32 v[24:25], v[24:25], v[234:235], v[234:235] op_sel:[0,0,1] op_sel_hi:[1,0,1]
	v_mul_f32_e32 v42, v38, v39
	v_rcp_f32_e32 v42, v42
	v_pk_mul_f32 v[44:45], v[24:25], s[18:19] op_sel_hi:[1,0]
	v_exp_f32_e32 v44, v44
	v_exp_f32_e32 v45, v45
	v_pk_mul_f32 v[38:39], v[38:39], v[42:43] op_sel:[1,0] op_sel_hi:[0,0]
	v_pk_mul_f32 v[26:27], v[26:27], v[38:39]
	v_pk_fma_f32 v[30:31], v[86:87], v[242:243], v[218:219] op_sel_hi:[1,0,1] clamp
	v_pk_add_f32 v[38:39], v[44:45], 1.0 op_sel_hi:[1,0]
	v_mul_f32_e32 v42, v38, v39
	v_rcp_f32_e32 v42, v42
	v_pk_mul_f32 v[26:27], v[34:35], v[26:27]
; __device__ __forceinline__ unsigned pk4_fp8(float a, float b, float c, float d) { int w = __builtin_amdgcn_cvt_pk_fp8_f32(a, b, 0, false); w = __builtin_amdgcn_cvt_pk_fp8_f32(c, d, w, true); return (unsigned)w; }
;     static __device__ __forceinline__ f32x2 act2(f32x2 g, f32x2 u) {
;         g.x = __builtin_amdgcn_fmed3f(g.x, -24.0f, 7.0f); g.y = __builtin_amdgcn_fmed3f(g.y, -24.0f, 7.0f);
;         u.x = __builtin_amdgcn_fmed3f(u.x, -7.0f, 7.0f); u.y = __builtin_amdgcn_fmed3f(u.y, -7.0f, 7.0f);
;         f32x2 z = g * (-1.702f * 1.4426950408889634f);
;         f32x2 d; d.x = __builtin_amdgcn_exp2f(z.x); d.y = __builtin_amdgcn_exp2f(z.y);
;         d = d + 1.0f;
;         const float r = __builtin_amdgcn_rcpf(d.x * d.y);
;         f32x2 sg; sg.x = r * d.y; sg.y = r * d.x;
;         return (u + 1.0f) * (g * sg);
;     }
;     __device__ __forceinline__ void operator()(const f32x4 (&acc)[2][2][4][2], const pg8::Unit& u, int wr, int wc, int fr, int fq) const {
;         const int e = u.aux;
;         unsigned char* Ht = ws + WS_H2 + (size_t)u.pm * TSF8;
;         const int hc = u.pn * 128 + wc * 32 + 8 * fq;
;         const f32x4 bg0 = *(const f32x4*)(bgate + e * FF + hc), bg1 = *(const f32x4*)(bgate + e * FF + hc + 4);
;         const f32x4 bu0 = *(const f32x4*)(bup + e * FF + hc), bu1 = *(const f32x4*)(bup + e * FF + hc + 4);
; #pragma unroll
;         for (int ai = 0; ai < 2; ++ai)
; #pragma unroll
;             for (int m = 0; m < 4; ++m) { const int rl = ai * 128 + wr * 64 + m * 16 + fr;
;                 const f32x4 g0 = acc[ai][0][m][0] * (1.0f / 64.0f) + bg0, g1 = acc[ai][0][m][1] * (1.0f / 64.0f) + bg1, u0 = acc[ai][1][m][0] * (1.0f / 64.0f) + bu0, u1 = acc[ai][1][m][1] * (1.0f / 64.0f) + bu1;
;                 const f32x2 h0 = act2((f32x2){g0[0], g0[1]}, (f32x2){u0[0], u0[1]}), h1 = act2((f32x2){g0[2], g0[3]}, (f32x2){u0[2], u0[3]});
;                 const f32x2 h2 = act2((f32x2){g1[0], g1[1]}, (f32x2){u1[0], u1[1]}), h3 = act2((f32x2){g1[2], g1[3]}, (f32x2){u1[2], u1[3]});
;                 *(u32x2*)(Ht + (size_t)rl * FF + hc) = (u32x2){pk4_fp8(h0.x, h0.y, h1.x, h1.y), pk4_fp8(h2.x, h2.y, h3.x, h3.y)}; }
	v_pk_fma_f32 v[30:31], v[30:31], v[234:235], v[234:235] op_sel:[0,0,1] op_sel_hi:[1,0,1]
	v_pk_mul_f32 v[34:35], v[38:39], v[42:43] op_sel:[1,0] op_sel_hi:[0,0]
	v_pk_mul_f32 v[24:25], v[24:25], v[34:35]
	v_pk_mul_f32 v[34:35], v[30:31], s[18:19] op_sel_hi:[1,0]
	v_pk_fma_f32 v[32:33], v[100:101], v[242:243], v[228:229] op_sel:[0,1,0] op_sel_hi:[1,1,1] clamp
	v_exp_f32_e32 v34, v34
	v_exp_f32_e32 v35, v35
	v_pk_fma_f32 v[28:29], v[88:89], v[242:243], v[220:221] op_sel_hi:[1,0,1] clamp
	v_pk_fma_f32 v[32:33], v[32:33], v[236:237], v[236:237] op_sel:[0,0,1] op_sel_hi:[1,0,1]
	v_pk_add_f32 v[34:35], v[34:35], 1.0 op_sel_hi:[1,0]
	v_pk_fma_f32 v[40:41], v[94:95], v[242:243], v[214:215] op_sel:[0,1,0] op_sel_hi:[1,1,1] clamp
	v_mul_f32_e32 v38, v34, v35
	v_pk_fma_f32 v[28:29], v[28:29], v[234:235], v[234:235] op_sel:[0,0,1] op_sel_hi:[1,0,1]
	v_pk_mul_f32 v[24:25], v[32:33], v[24:25]
	v_pk_fma_f32 v[32:33], v[40:41], v[236:237], v[236:237] op_sel:[0,0,1] op_sel_hi:[1,0,1]
	v_rcp_f32_e32 v38, v38
	v_pk_mul_f32 v[40:41], v[28:29], s[18:19] op_sel_hi:[1,0]
	v_pk_fma_f32 v[36:37], v[96:97], v[242:243], v[216:217] op_sel:[0,1,0] op_sel_hi:[1,1,1] clamp
	v_exp_f32_e32 v40, v40
	v_exp_f32_e32 v41, v41
	v_pk_mul_f32 v[34:35], v[34:35], v[38:39] op_sel:[1,0] op_sel_hi:[0,0]
	v_pk_mul_f32 v[30:31], v[30:31], v[34:35]
	v_pk_add_f32 v[34:35], v[40:41], 1.0 op_sel_hi:[1,0]
	v_pk_mul_f32 v[30:31], v[32:33], v[30:31]
	v_mul_f32_e32 v38, v34, v35
	v_rcp_f32_e32 v38, v38
	v_pk_fma_f32 v[32:33], v[36:37], v[236:237], v[236:237] op_sel:[0,0,1] op_sel_hi:[1,0,1]
	v_mov_b32_e32 v36, v198
	v_mov_b32_e32 v37, v198
	v_cvt_pk_fp8_f32 v36, v26, v27
	v_cvt_pk_fp8_f32 v37, v30, v31
	v_pk_mul_f32 v[34:35], v[34:35], v[38:39] op_sel:[1,0] op_sel_hi:[0,0]
	v_pk_mul_f32 v[26:27], v[28:29], v[34:35]
	v_cvt_pk_fp8_f32 v36, v24, v25 op_sel:[0,0,1]
	v_pk_mul_f32 v[26:27], v[32:33], v[26:27]
	v_add_co_u32_e32 v24, vcc, s60, v22
	v_cvt_pk_fp8_f32 v37, v26, v27 op_sel:[0,0,1]
	v_pk_fma_f32 v[14:15], v[74:75], v[242:243], v[222:223] op_sel_hi:[1,0,1] clamp
	v_addc_co_u32_e32 v25, vcc, 0, v23, vcc
	v_pk_fma_f32 v[14:15], v[14:15], v[234:235], v[234:235] op_sel:[0,0,1] op_sel_hi:[1,0,1]
	global_store_dwordx2 v[24:25], v[36:37], off
	v_pk_mul_f32 v[24:25], v[14:15], s[18:19] op_sel_hi:[1,0]
	v_pk_fma_f32 v[16:17], v[76:77], v[242:243], v[224:225] op_sel_hi:[1,0,1] clamp
	v_exp_f32_e32 v24, v24
	v_exp_f32_e32 v25, v25
	v_pk_fma_f32 v[16:17], v[16:17], v[234:235], v[234:235] op_sel:[0,0,1] op_sel_hi:[1,0,1]
	v_pk_mul_f32 v[28:29], v[16:17], s[18:19] op_sel_hi:[1,0]
	v_pk_add_f32 v[24:25], v[24:25], 1.0 op_sel_hi:[1,0]
	v_exp_f32_e32 v28, v28
	v_mul_f32_e32 v26, v24, v25
	v_rcp_f32_e32 v26, v26
	v_exp_f32_e32 v29, v29
	v_pk_fma_f32 v[18:19], v[82:83], v[242:243], v[226:227] op_sel:[0,1,0] op_sel_hi:[1,1,1] clamp
	v_pk_fma_f32 v[10:11], v[70:71], v[242:243], v[218:219] op_sel_hi:[1,0,1] clamp
	v_pk_mul_f32 v[24:25], v[24:25], v[26:27] op_sel:[1,0] op_sel_hi:[0,0]
	v_pk_mul_f32 v[14:15], v[14:15], v[24:25]
	v_pk_add_f32 v[24:25], v[28:29], 1.0 op_sel_hi:[1,0]
	v_pk_fma_f32 v[18:19], v[18:19], v[236:237], v[236:237] op_sel:[0,0,1] op_sel_hi:[1,0,1]
	v_mul_f32_e32 v26, v24, v25
	v_rcp_f32_e32 v26, v26
	v_pk_fma_f32 v[20:21], v[84:85], v[242:243], v[228:229] op_sel:[0,1,0] op_sel_hi:[1,1,1] clamp
	v_pk_fma_f32 v[10:11], v[10:11], v[234:235], v[234:235] op_sel:[0,0,1] op_sel_hi:[1,0,1]
	v_pk_mul_f32 v[14:15], v[18:19], v[14:15]
	v_pk_fma_f32 v[18:19], v[20:21], v[236:237], v[236:237] op_sel:[0,0,1] op_sel_hi:[1,0,1]
	v_pk_mul_f32 v[20:21], v[24:25], v[26:27] op_sel:[1,0] op_sel_hi:[0,0]
	v_pk_mul_f32 v[16:17], v[16:17], v[20:21]
	v_pk_mul_f32 v[20:21], v[10:11], s[18:19] op_sel_hi:[1,0]
	v_exp_f32_e32 v20, v20
	v_exp_f32_e32 v21, v21
	v_pk_fma_f32 v[12:13], v[72:73], v[242:243], v[220:221] op_sel_hi:[1,0,1] clamp
	v_pk_mul_f32 v[16:17], v[18:19], v[16:17]
	v_pk_fma_f32 v[12:13], v[12:13], v[234:235], v[234:235] op_sel:[0,0,1] op_sel_hi:[1,0,1]
	v_pk_add_f32 v[18:19], v[20:21], 1.0 op_sel_hi:[1,0]
	v_mul_f32_e32 v20, v18, v19
	v_rcp_f32_e32 v20, v20
	v_pk_mul_f32 v[24:25], v[12:13], s[18:19] op_sel_hi:[1,0]
	v_pk_fma_f32 v[6:7], v[78:79], v[242:243], v[214:215] op_sel:[0,1,0] op_sel_hi:[1,1,1] clamp
	v_exp_f32_e32 v24, v24
	v_exp_f32_e32 v25, v25
	v_pk_mul_f32 v[18:19], v[18:19], v[20:21] op_sel:[1,0] op_sel_hi:[0,0]
	v_pk_mul_f32 v[10:11], v[10:11], v[18:19]
	v_pk_fma_f32 v[6:7], v[6:7], v[236:237], v[236:237] op_sel:[0,0,1] op_sel_hi:[1,0,1]
	v_pk_add_f32 v[18:19], v[24:25], 1.0 op_sel_hi:[1,0]
	v_mul_f32_e32 v20, v18, v19
	v_rcp_f32_e32 v20, v20
	v_pk_fma_f32 v[8:9], v[80:81], v[242:243], v[216:217] op_sel:[0,1,0] op_sel_hi:[1,1,1] clamp
	v_pk_mul_f32 v[6:7], v[6:7], v[10:11]
	v_pk_mul_f32 v[10:11], v[18:19], v[20:21] op_sel:[1,0] op_sel_hi:[0,0]
	v_mov_b32_e32 v18, v198
	v_mov_b32_e32 v19, v198
	v_cvt_pk_fp8_f32 v18, v14, v15
	v_cvt_pk_fp8_f32 v19, v6, v7
	v_pk_fma_f32 v[8:9], v[8:9], v[236:237], v[236:237] op_sel:[0,0,1] op_sel_hi:[1,0,1]
	v_pk_mul_f32 v[6:7], v[12:13], v[10:11]
	v_cvt_pk_fp8_f32 v18, v16, v17 op_sel:[0,0,1]
	v_pk_mul_f32 v[6:7], v[8:9], v[6:7]
	s_nop 0
	v_cvt_pk_fp8_f32 v19, v6, v7 op_sel:[0,0,1]
	v_add_co_u32_e32 v6, vcc, 0x2c000, v22
	s_nop 1
	v_addc_co_u32_e32 v7, vcc, 0, v23, vcc
	s_and_b64 vcc, exec, s[2:3]
	s_mov_b64 s[2:3], -1
	global_store_dwordx2 v[6:7], v[18:19], off
	s_cbranch_vccnz .LBB0_956
	s_andn2_b64 vcc, exec, s[10:11]
	s_mov_b64 s[22:23], s[8:9]
	s_mov_b64 s[24:25], s[20:21]
	s_cbranch_vccnz .LBB0_972
	s_lshl_b32 s2, s41, 3
	s_add_i32 s2, s2, s39
	s_ashr_i32 s3, s2, 31
	s_lshl_b64 s[2:3], s[2:3], 18
	s_add_u32 s22, s37, s2
	s_addc_u32 s23, s38, s3
	s_mov_b64 s[24:25], s[6:7]
